# speedup vs baseline: 1.0691x; 1.0198x over previous
_Z11main_kernelPKfPKiPK15HIP_vector_typeIjLj4EES0_PfS7_S2_i:
	v_and_b32_e32 v104, 0x3ff, v0
	s_mul_i32 s2, s2, 12
	v_readfirstlane_b32 s3, v104
	s_lshr_b32 s3, s3, 6
	s_add_i32 s2, s3, s2
	s_load_dwordx8 s[12:19], s[0:1], 0x0
	s_load_dwordx2 s[10:11], s[0:1], 0x30
	s_mul_i32 s2, s2, 0xf424
	s_mul_hi_u32 s4, s2, 0xaaaaaaab
	s_add_i32 s2, s2, 0xf424
	s_mul_hi_u32 s2, s2, 0xaaaaaaab
	s_lshr_b32 s42, s2, 11
	s_lshl_b32 s2, s3, 8
	v_and_b32_e32 v1, 15, v0
	v_bfe_u32 v112, v0, 4, 2
	s_lshr_b32 s44, s4, 11
	s_lshl_b32 s33, s3, 13
	s_add_i32 s43, s2, 0x20000
	s_sub_u32 s60, s42, s44
	s_cmp_lt_u32 s60, 21
	s_cbranch_scc1 .Lmain_noprio
	s_setprio 2
.Lmain_noprio:
	s_waitcnt lgkmcnt(0)
	s_and_b32 s13, s13, 0xffff
	v_lshlrev_b32_e32 v105, 9, v112
	v_lshlrev_b32_e32 v2, 6, v112
	v_lshlrev_b32_e32 v3, 4, v1
	s_cmp_lt_u32 s44, s42
	s_mov_b32 s7, 0x20000
	v_bitop3_b32 v113, v2, v105, v3 bitop3:0xde
	s_mov_b32 s6, 0x1e848000
	s_cselect_b64 s[8:9], -1, 0
	v_lshlrev_b32_e32 v102, 2, v1
	v_lshlrev_b32_e32 v14, 4, v104
	v_mov_b32_e32 v15, 0
	v_lshl_add_u64 v[6:7], s[16:17], 0, v[14:15]
	v_add_co_u32_e32 v16, vcc, 0x3000, v6
	v_min_u32_e32 v6, 0x1ff, v104
	s_nop 0
	v_addc_co_u32_e32 v17, vcc, 0, v7, vcc
	v_lshlrev_b32_e32 v7, 2, v6
	global_load_dword v15, v7, s[10:11]
	global_load_dwordx4 v[2:5], v14, s[16:17]
	v_lshlrev_b32_e32 v18, 4, v6
	v_or_b32_e32 v19, 0x6000, v18
	global_load_dwordx4 v[6:9], v[16:17], off
	global_load_dwordx4 v[10:13], v19, s[16:17]
	v_min_u32_e32 v16, 0x17f, v104
	v_lshlrev_b32_e32 v16, 2, v16
	global_load_dword v17, v16, s[18:19]
	s_cmp_ge_u32 s44, s42
	s_cbranch_scc1 .Lmain_nodma
	s_lshl_b32 s2, s44, 13
	s_add_i32 m0, s33, 0x8000
	s_mov_b32 s4, s12
	s_mov_b32 s5, s13
	buffer_load_dwordx4 v113, s[4:7], s2 offen nt lds
	s_add_i32 m0, s33, 0x8400
	s_or_b32 s3, s2, 0x800
	buffer_load_dwordx4 v113, s[4:7], s3 offen nt lds
	s_add_i32 m0, s33, 0x8800
	s_or_b32 s3, s2, 0x1000
	buffer_load_dwordx4 v113, s[4:7], s3 offen nt lds
	s_add_i32 m0, s33, 0x8c00
	s_or_b32 s3, s2, 0x1800
	buffer_load_dwordx4 v113, s[4:7], s3 offen nt lds
	s_add_i32 m0, s33, 0x9000
	s_or_b32 s3, s2, 0x100
	buffer_load_dwordx4 v113, s[4:7], s3 offen nt lds
	s_add_i32 m0, s33, 0x9400
	s_or_b32 s3, s2, 0x900
	buffer_load_dwordx4 v113, s[4:7], s3 offen nt lds
	s_add_i32 m0, s33, 0x9800
	s_or_b32 s3, s2, 0x1100
	buffer_load_dwordx4 v113, s[4:7], s3 offen nt lds
	s_add_i32 m0, s33, 0x9c00
	s_or_b32 s2, s2, 0x1900
	buffer_load_dwordx4 v113, s[4:7], s2 offen nt lds
	s_lshl_b32 s2, s44, 6
	s_add_u32 s2, s14, s2
	s_addc_u32 s3, s15, 0
	s_mov_b32 m0, s43
	s_nop 0
	global_load_lds_dword v102, s[2:3]

.LBB1_53:
	s_waitcnt vmcnt(0)
	v_cmp_ne_u32_e32 vcc, 0, v0
	s_lshr_b32 s0, vcc_lo, 16
	s_lshr_b32 s1, vcc_hi, 16
	s_or_b32 s0, s0, vcc_lo
	s_or_b32 s1, s1, vcc_hi
	s_or_b32 s0, s0, s1
	s_and_b32 s0, s0, 0xffff
	s_cmp_eq_u32 s0, 0
	s_cbranch_scc1 .LBB1_104
	v_lshrrev_b32_e64 v1, v100, s0
	v_and_b32_e32 v3, 15, v101
	v_and_b32_e32 v1, 1, v1
	v_add_u32_e32 v2, s16, v3
	v_cmp_ne_u32_e64 s[2:3], 0, v1
	v_cmp_eq_u32_e64 s[6:7], s45, v2
	v_cmp_eq_u32_e64 s[8:9], s46, v2
	s_and_b32 s38, s2, 0xffff
	s_flbit_i32_b32 s4, s38
	s_sub_u32 s5, 31, s4
	s_or_b64 s[6:7], s[6:7], s[8:9]
	v_cmp_le_u32_e64 s[12:13], s5, v3
	s_or_b64 s[6:7], s[6:7], s[20:21]
	v_add3_u32 v3, s33, v105, v102
	s_or_b64 s[6:7], s[6:7], s[12:13]
	s_and_b32 s1, s6, s38
	s_andn2_b32 s3, s38, s1
	v_add_u32_e32 v36, 0x8000, v3
	v_add_u32_e32 v37, 0x8800, v3
	v_add_u32_e32 v38, 0x9000, v3
	v_add_u32_e32 v39, 0x9800, v3
	ds_write2_b32 v36, v32, v28 offset1:16
	ds_write2_b32 v36, v24, v20 offset0:32 offset1:48
	ds_write2_b32 v36, v16, v12 offset0:64 offset1:80
	ds_write2_b32 v36, v8, v4 offset0:96 offset1:112
	ds_write2_b32 v37, v33, v29 offset1:16
	ds_write2_b32 v37, v25, v21 offset0:32 offset1:48
	ds_write2_b32 v37, v17, v13 offset0:64 offset1:80
	ds_write2_b32 v37, v9, v5 offset0:96 offset1:112
	ds_write2_b32 v38, v34, v30 offset1:16
	ds_write2_b32 v38, v26, v22 offset0:32 offset1:48
	ds_write2_b32 v38, v18, v14 offset0:64 offset1:80
	ds_write2_b32 v38, v10, v6 offset0:96 offset1:112
	ds_write2_b32 v39, v35, v31 offset1:16
	ds_write2_b32 v39, v27, v23 offset0:32 offset1:48
	ds_write2_b32 v39, v19, v15 offset0:64 offset1:80
	ds_write2_b32 v39, v11, v7 offset0:96 offset1:112
	s_mov_b32 s17, 0
	s_lshl_b64 s[14:15], s[16:17], 9
	s_add_u32 s14, s18, s14
	s_addc_u32 s15, s19, s15
	s_add_u32 s22, s14, 0x1000
	s_addc_u32 s23, s15, 0
	v_lshlrev_b32_e32 v40, 2, v101
	v_add_u32_e32 v41, s33, v40
	v_and_b32_e32 v2, 31, v101
	v_lshrrev_b32_e32 v1, 5, v101
	v_lshlrev_b32_e32 v2, 4, v2
	v_lshl_add_u32 v42, v1, 9, v2
	v_add_u32_e32 v43, s33, v42
	v_lshrrev_b32_e64 v76, v1, s3
	s_waitcnt lgkmcnt(0)
	ds_read_b128 v[44:47], v43 offset:32768
	ds_read_b128 v[48:51], v43 offset:33792
	ds_read_b128 v[52:55], v43 offset:34816
	ds_read_b128 v[56:59], v43 offset:35840
	ds_read_b128 v[60:63], v43 offset:36864
	ds_read_b128 v[64:67], v43 offset:37888
	ds_read_b128 v[68:71], v43 offset:38912
	ds_read_b128 v[72:75], v43 offset:39936
	v_cmp_ne_u32_e32 vcc, 0, v0
	s_and_saveexec_b64 s[24:25], vcc
	s_cbranch_execz .Lfl_nocnt
	s_mov_b32 s2, 0x24924925
	v_mul_hi_u32 v1, v0, s2
	v_sub_u32_e32 v0, v0, v1
	v_lshrrev_b32_e32 v0, 1, v0
	v_add_u32_e32 v0, v0, v1
	v_lshrrev_b32_e32 v0, 2, v0
	v_cvt_f32_u32_e32 v0, v0
	s_lshl_b64 s[26:27], s[16:17], 2
	s_add_u32 s26, s10, s26
	s_addc_u32 s27, s11, s27
	v_lshlrev_b32_e32 v1, 2, v100
	global_atomic_add_f32 v1, v0, s[26:27]
.Lfl_nocnt:
	s_or_b64 exec, exec, s[24:25]
.Lfl_sh:
	s_cmp_eq_u32 s1, 0
	s_cbranch_scc1 .Lfl_priv
	s_ff1_i32_b32 s4, s1
	s_bitset0_b32 s1, s4
	s_lshl_b32 s5, s4, 9
	v_add_u32_e32 v1, s5, v41
	ds_read2st64_b32 v[4:5], v1 offset0:128 offset1:129
	s_add_u32 s6, s14, s5
	s_addc_u32 s7, s15, 0
	s_waitcnt lgkmcnt(0)
	global_atomic_add_f32 v40, v4, s[6:7]
	global_atomic_add_f32 v40, v5, s[6:7] offset:256
	s_branch .Lfl_sh
.Lfl_priv:
	s_cmp_eq_u32 s3, 0
	s_cbranch_scc1 .LBB1_104
	s_waitcnt lgkmcnt(0)
	v_and_b32_e32 v77, 1, v76
	v_cmp_ne_u32_e32 vcc, 0, v77
	s_and_b64 exec, exec, vcc
	global_store_dwordx4 v42, v[44:47], s[14:15] sc1
	s_mov_b64 exec, -1
	v_and_b32_e32 v77, 4, v76
	v_cmp_ne_u32_e32 vcc, 0, v77
	s_and_b64 exec, exec, vcc
	global_store_dwordx4 v42, v[48:51], s[14:15] offset:1024 sc1
	s_mov_b64 exec, -1
	v_and_b32_e32 v77, 16, v76
	v_cmp_ne_u32_e32 vcc, 0, v77
	s_and_b64 exec, exec, vcc
	global_store_dwordx4 v42, v[52:55], s[14:15] offset:2048 sc1
	s_mov_b64 exec, -1
	v_and_b32_e32 v77, 64, v76
	v_cmp_ne_u32_e32 vcc, 0, v77
	s_and_b64 exec, exec, vcc
	global_store_dwordx4 v42, v[56:59], s[14:15] offset:3072 sc1
	s_mov_b64 exec, -1
	v_and_b32_e32 v77, 256, v76
	v_cmp_ne_u32_e32 vcc, 0, v77
	s_and_b64 exec, exec, vcc
	global_store_dwordx4 v42, v[60:63], s[22:23] sc1
	s_mov_b64 exec, -1
	v_and_b32_e32 v77, 1024, v76
	v_cmp_ne_u32_e32 vcc, 0, v77
	s_and_b64 exec, exec, vcc
	global_store_dwordx4 v42, v[64:67], s[22:23] offset:1024 sc1
	s_mov_b64 exec, -1
	v_and_b32_e32 v77, 4096, v76
	v_cmp_ne_u32_e32 vcc, 0, v77
	s_and_b64 exec, exec, vcc
	global_store_dwordx4 v42, v[68:71], s[22:23] offset:2048 sc1
	s_mov_b64 exec, -1
	v_and_b32_e32 v77, 16384, v76
	v_cmp_ne_u32_e32 vcc, 0, v77
	s_and_b64 exec, exec, vcc
	global_store_dwordx4 v42, v[72:75], s[22:23] offset:3072 sc1
	s_mov_b64 exec, -1
